# baseline (speedup 1.0000x reference)
_Z8dog_mainPKfS0_S0_S0_S0_S0_S0_Pf:
	s_load_dwordx8 s[12:19], s[0:1], 0x0
	s_load_dwordx8 s[20:27], s[0:1], 0x20
	s_and_b32 s3, s2, 7
	s_lshl_b32 s3, s3, 5
	s_lshr_b32 s4, s2, 3
	s_add_i32 s4, s3, s4
	s_and_b32 s6, s4, 3
	s_lshr_b32 s7, s4, 2
	s_mov_b32 s5, 0
	s_lshl_b64 s[8:9], s[4:5], 18
	v_and_b32_e32 v1, 63, v0
	v_lshrrev_b32_e32 v2, 6, v0
	v_and_b32_e32 v3, 15, v0
	v_and_b32_e32 v7, 31, v0
	v_lshl_or_b32 v5, v2, 5, v7
	v_lshlrev_b32_e32 v5, 2, v5
	v_mov_b32_e32 v4, v5
	v_lshlrev_b32_e32 v6, 4, v1
	v_lshl_or_b32 v6, v2, 12, v6
	v_bfe_u32 v7, v0, 4, 2
	s_waitcnt lgkmcnt(0)
	s_add_u32 s12, s12, s8
	s_addc_u32 s13, s13, s9
	global_load_dwordx4 v[128:131], v6, s[12:13] offset:0 nt
	global_load_dwordx4 v[132:135], v6, s[12:13] offset:1024 nt
	global_load_dwordx4 v[136:139], v6, s[12:13] offset:2048 nt
	global_load_dwordx4 v[140:143], v6, s[12:13] offset:3072 nt
	v_add_u32_e32 v6, 0x8000, v6
	global_load_dwordx4 v[144:147], v6, s[12:13] offset:0 nt
	global_load_dwordx4 v[148:151], v6, s[12:13] offset:1024 nt
	global_load_dwordx4 v[152:155], v6, s[12:13] offset:2048 nt
	global_load_dwordx4 v[156:159], v6, s[12:13] offset:3072 nt
	global_load_dword v32, v4, s[18:19]
	global_load_dword v33, v4, s[20:21]
	global_load_dword v34, v4, s[22:23]
	global_load_dword v35, v4, s[24:25]
	global_load_dword v36, v4, s[14:15]
	global_load_dword v37, v4, s[16:17]
	v_and_b32_e32 v16, 1, v0
	v_cmp_eq_u32_e64 s[30:31], 0, v16
	v_and_b32_e32 v17, 2, v0
	v_cmp_eq_u32_e64 s[32:33], 0, v17
	v_and_b32_e32 v16, 3, v0
	v_lshrrev_b32_e32 v17, 2, v1
	v_lshlrev_b32_e32 v16, 5, v16
	v_lshl_add_u32 v16, v17, 1, v16
	v_lshrrev_b32_e32 v17, 1, v2
	s_movk_i32 s10, 0x110
	v_mad_u32_u24 v16, v17, s10, v16
	v_and_b32_e32 v17, 1, v2
	v_lshl_add_u32 v14, v17, 7, v16
	v_lshlrev_b32_e32 v17, 4, v7
	v_mad_u32_u24 v15, v3, s10, v17
	s_lshl_b32 s11, s6, 5
	v_lshl_add_u32 v18, v7, 2, s11
	v_cvt_f32_u32_e32 v18, v18
	v_lshlrev_b32_e32 v19, 3, v7
	v_cvt_f32_u32_e32 v19, v19
	s_waitcnt vmcnt(0)
	v_lshlrev_b32_e32 v16, 2, v3
	v_add_u32_e32 v17, 64, v16
	ds_bpermute_b32 v40, v16, v32
	ds_bpermute_b32 v46, v17, v32
	ds_bpermute_b32 v41, v16, v33
	ds_bpermute_b32 v47, v17, v33
	ds_bpermute_b32 v42, v16, v34
	ds_bpermute_b32 v48, v17, v34
	ds_bpermute_b32 v43, v16, v35
	ds_bpermute_b32 v49, v17, v35
	ds_bpermute_b32 v44, v16, v36
	ds_bpermute_b32 v50, v17, v36
	ds_bpermute_b32 v45, v16, v37
	ds_bpermute_b32 v51, v17, v37
	s_waitcnt lgkmcnt(0)
	v_add_f32_e32 v41, v40, v41
	v_sub_f32_e32 v12, v19, v42
	v_sub_f32_e32 v13, v18, v43
	v_rcp_f32_e32 v42, v40
	v_rcp_f32_e32 v43, v41
	s_nop 0
	v_fma_f32 v20, -v40, v42, 1.0
	v_fma_f32 v42, v20, v42, v42
	v_fma_f32 v20, -v41, v43, 1.0
	v_fma_f32 v43, v20, v43, v43
	v_mul_f32_e32 v8, 0xbf38aa3b, v42
	v_mul_f32_e32 v9, 0xbf38aa3b, v43
	v_mul_f32_e32 v44, v44, v42
	v_mul_f32_e32 v45, v45, v43
	v_mul_f32_e32 v10, 0x3e22f983, v44
	v_mul_f32_e32 v11, 0x3e22f983, v45
	v_add_f32_e32 v47, v46, v47
	v_sub_f32_e32 v2, v19, v48
	v_sub_f32_e32 v3, v18, v49
	v_rcp_f32_e32 v48, v46
	v_rcp_f32_e32 v49, v47
	s_nop 0
	v_fma_f32 v20, -v46, v48, 1.0
	v_fma_f32 v48, v20, v48, v48
	v_fma_f32 v20, -v47, v49, 1.0
	v_fma_f32 v49, v20, v49, v49
	v_mul_f32_e32 v28, 0xbf38aa3b, v48
	v_mul_f32_e32 v29, 0xbf38aa3b, v49
	v_mul_f32_e32 v50, v50, v48
	v_mul_f32_e32 v51, v51, v49
	v_mul_f32_e32 v30, 0x3e22f983, v50
	v_mul_f32_e32 v31, 0x3e22f983, v51
	s_getpc_b64 s[44:45]
